# P6 clean-ups stacked: v100 (mods loads in flight, drain moved behind the top-k) + DPP/permlane wave sums in P6 and P10
# speedup vs baseline: 1.0008x; 1.0005x over previous
.LBB0_986:
	v_mov_b32_e32 v246, v191
	v_mov_b32_e32 v247, v192
	v_mov_b32_e32 v248, v190
	v_mov_b32_e32 v249, v193
	v_pk_add_f32 v[246:247], v[246:247], v[248:249]
	v_mov_b32_e32 v248, v187
	v_mov_b32_e32 v249, v188
	v_mov_b32_e32 v216, v186
	v_mov_b32_e32 v217, v189
	v_pk_add_f32 v[216:217], v[248:249], v[216:217]
	v_add_f32_e32 v209, v246, v247
	v_pk_add_f32 v[216:217], v[216:217], v[216:217] op_sel:[0,1] op_sel_hi:[1,0]
	v_add_f32_e32 v246, 0, v209
	v_add_f32_e32 v248, v182, v183
	v_add_f32_e32 v218, v184, v185
	v_mov_b32_e32 v247, v178
	v_mov_b32_e32 v217, v179
	v_mov_b32_e32 v249, v180
	v_mov_b32_e32 v219, v181
	v_pk_add_f32 v[216:217], v[246:247], v[216:217]
	v_pk_add_f32 v[218:219], v[248:249], v[218:219]
	s_mov_b32 s36, 0xf800000
	v_pk_add_f32 v[216:217], v[216:217], v[218:219]
	s_nop 0
	v_add_f32_e32 v209, v216, v217
	s_nop 1
	v_add_f32_dpp v209, v209, v209 quad_perm:[1,0,3,2] row_mask:0xf bank_mask:0xf
	s_nop 1
	v_add_f32_dpp v209, v209, v209 quad_perm:[2,3,0,1] row_mask:0xf bank_mask:0xf
	s_nop 1
	v_add_f32_dpp v209, v209, v209 row_half_mirror row_mask:0xf bank_mask:0xf
	s_nop 1
	v_add_f32_dpp v209, v209, v209 row_mirror row_mask:0xf bank_mask:0xf
	v_mov_b32_e32 v216, v209
	s_nop 1
	v_permlane16_swap_b32_e32 v216, v209
	s_nop 1
	v_add_f32_e32 v209, v209, v216
	v_mov_b32_e32 v216, v209
	s_nop 1
	v_permlane32_swap_b32_e32 v216, v209
	s_nop 1
	v_add_f32_e32 v209, v209, v216
	v_fmamk_f32 v191, v209, 0xba800000, v191
	v_fmamk_f32 v190, v209, 0xba800000, v190
	v_fmamk_f32 v193, v209, 0xba800000, v193
	v_fmac_f32_e32 v192, 0xba800000, v209
	v_pk_mul_f32 v[216:217], v[192:193], v[192:193]
	v_pk_mul_f32 v[218:219], v[190:191], v[190:191]
	v_fmamk_f32 v187, v209, 0xba800000, v187
	v_fmamk_f32 v186, v209, 0xba800000, v186
	v_fmamk_f32 v189, v209, 0xba800000, v189
	v_pk_mov_b32 v[246:247], v[218:219], v[216:217] op_sel:[1,0]
	v_mov_b32_e32 v219, v217
	v_fmac_f32_e32 v188, 0xba800000, v209
	v_pk_add_f32 v[216:217], v[246:247], v[218:219]
	v_pk_mul_f32 v[218:219], v[188:189], v[188:189]
	v_pk_mul_f32 v[246:247], v[186:187], v[186:187]
	v_fmac_f32_e32 v184, 0xba800000, v209
	v_pk_mov_b32 v[248:249], v[246:247], v[218:219] op_sel:[1,0]
	v_mov_b32_e32 v247, v219
	v_pk_add_f32 v[218:219], v[248:249], v[246:247]
	v_fmamk_f32 v246, v209, 0xba800000, v182
	v_fmamk_f32 v247, v209, 0xba800000, v183
	v_mul_f32_e32 v182, v246, v246
	v_pk_fma_f32 v[182:183], v[246:247], v[246:247], v[182:183] op_sel_hi:[1,1,0]
	v_fmamk_f32 v185, v209, 0xba800000, v185
	v_mul_f32_e32 v182, v184, v184
	v_pk_add_f32 v[216:217], v[216:217], v[216:217] op_sel_hi:[0,1]
	v_pk_add_f32 v[218:219], v[218:219], v[218:219] op_sel_hi:[0,1]
	v_pk_fma_f32 v[248:249], v[184:185], v[184:185], v[182:183] op_sel_hi:[1,1,0]
	v_fmamk_f32 v181, v209, 0xba800000, v181
	v_fmamk_f32 v180, v209, 0xba800000, v180
	v_fmamk_f32 v179, v209, 0xba800000, v179
	v_fmac_f32_e32 v178, 0xba800000, v209
	v_mul_f32_e32 v182, v178, v178
	v_mul_f32_e32 v248, v179, v179
	v_mul_f32_e32 v216, v180, v180
	v_mul_f32_e32 v218, v181, v181
	v_pk_add_f32 v[182:183], v[182:183], v[248:249]
	v_pk_add_f32 v[216:217], v[216:217], v[218:219]
	s_nop 0
	v_pk_add_f32 v[182:183], v[182:183], v[216:217]
	s_nop 0
	v_add_f32_e32 v182, v182, v183
	s_nop 1
	v_add_f32_dpp v182, v182, v182 quad_perm:[1,0,3,2] row_mask:0xf bank_mask:0xf
	s_nop 1
	v_add_f32_dpp v182, v182, v182 quad_perm:[2,3,0,1] row_mask:0xf bank_mask:0xf
	s_nop 1
	v_add_f32_dpp v182, v182, v182 row_half_mirror row_mask:0xf bank_mask:0xf
	s_nop 1
	v_add_f32_dpp v182, v182, v182 row_mirror row_mask:0xf bank_mask:0xf
	v_mov_b32_e32 v183, v182
	s_nop 1
	v_permlane16_swap_b32_e32 v183, v182
	s_nop 1
	v_add_f32_e32 v182, v182, v183
	v_mov_b32_e32 v183, v182
	s_nop 1
	v_permlane32_swap_b32_e32 v183, v182
	s_nop 1
	v_add_f32_e32 v182, v182, v183
	v_fmamk_f32 v182, v182, 0x3a800000, v211
	v_mul_f32_e32 v183, 0x4f800000, v182
	v_cmp_gt_f32_e32 vcc, s36, v182
	s_nop 1
	v_cndmask_b32_e32 v182, v182, v183, vcc
	v_sqrt_f32_e32 v183, v182
	s_nop 0
	v_add_u32_e32 v209, -1, v183
	v_add_u32_e32 v216, 1, v183
	v_fma_f32 v217, -v209, v183, v182
	v_fma_f32 v218, -v216, v183, v182
	v_cmp_ge_f32_e64 s[12:13], 0, v217
	s_nop 1
	v_cndmask_b32_e64 v183, v183, v209, s[12:13]
	v_cmp_lt_f32_e64 s[12:13], 0, v218
	s_nop 1
	v_cndmask_b32_e64 v183, v183, v216, s[12:13]
	v_mul_f32_e32 v209, 0x37800000, v183
	v_cndmask_b32_e32 v183, v183, v209, vcc
	v_cmp_class_f32_e32 vcc, v182, v212
	s_nop 1
	v_cndmask_b32_e32 v182, v183, v182, vcc
	v_div_scale_f32 v183, s[12:13], v182, v182, 1.0
	v_rcp_f32_e32 v209, v183
	v_readlane_b32 s12, v252, 4
	s_add_i32 s34, s12, s14
	s_ashr_i32 s35, s34, 31
	v_fma_f32 v216, -v183, v209, 1.0
	v_fmac_f32_e32 v209, v216, v209
	v_div_scale_f32 v216, vcc, 1.0, v182, 1.0
	v_mul_f32_e32 v217, v216, v209
	v_fma_f32 v218, -v183, v217, v216
	v_fmac_f32_e32 v217, v218, v209
	v_fma_f32 v183, -v183, v217, v216
	v_div_fmas_f32 v183, v183, v209, v217
	v_div_fixup_f32 v182, v183, v182, 1.0
	v_pk_mul_f32 v[190:191], v[190:191], v[182:183] op_sel_hi:[1,0]
	s_lshl_b64 s[12:13], s[34:35], 10
	s_waitcnt vmcnt(22)
	v_pk_fma_f32 v[190:191], v[2:3], v[190:191], v[6:7]
	v_pk_mul_f32 v[192:193], v[192:193], v[182:183] op_sel_hi:[1,0]
	v_pk_fma_f32 v[190:191], v[98:99], v[190:191], v[118:119]
	s_mov_b32 s35, 0xffff
	v_cvt_pk_bf16_f32 v216, v191, 0
	v_cvt_pk_bf16_f32 v183, v190, 0
	v_lshlrev_b32_e32 v216, 16, v216
	v_lshlrev_b32_e32 v209, 16, v183
	v_sub_f32_e32 v217, v191, v216
	v_and_or_b32 v216, v183, s35, v216
	v_mov_b32_e32 v183, v1
	v_cvt_pk_fp8_f32 v183, v190, v191
	v_pk_fma_f32 v[192:193], v[4:5], v[192:193], v[8:9]
	v_cvt_pk_bf16_f32 v218, v217, 0
	v_pk_fma_f32 v[192:193], v[100:101], v[192:193], v[120:121]
	v_sub_f32_e32 v209, v190, v209
	v_cvt_pk_fp8_f32 v183, v192, v193 op_sel:[0,0,1]
	v_cvt_pk_bf16_f32 v217, v192, 0
	v_cvt_pk_bf16_f32 v248, v193, 0
	v_lshlrev_b32_e32 v219, 16, v217
	v_lshlrev_b32_e32 v248, 16, v248
	v_sub_f32_e32 v219, v192, v219
	v_sub_f32_e32 v249, v193, v248
	v_lshl_add_u64 v[192:193], v[202:203], 0, s[12:13]
	global_store_dword v[192:193], v183, off
	v_add_u32_e32 v183, s47, v234
	v_pk_mul_f32 v[186:187], v[186:187], v[182:183] op_sel_hi:[1,0]
	v_cvt_pk_bf16_f32 v249, v249, 0
	s_waitcnt vmcnt(20)
	v_pk_fma_f32 v[186:187], v[10:11], v[186:187], v[18:19]
	v_cvt_pk_bf16_f32 v209, v209, 0
	v_cvt_pk_bf16_f32 v219, v219, 0
	v_and_or_b32 v217, v217, s35, v248
	v_lshlrev_b32_e32 v190, 16, v218
	v_lshlrev_b32_e32 v191, 16, v249
	v_pk_fma_f32 v[186:187], v[138:139], v[186:187], v[142:143]
	v_and_or_b32 v190, v209, s35, v190
	v_and_or_b32 v191, v219, s35, v191
	ds_write_b64 v183, v[216:217]
	ds_write_b64 v183, v[190:191] offset:33024
	v_pk_mul_f32 v[188:189], v[188:189], v[182:183] op_sel_hi:[1,0]
	v_cvt_pk_bf16_f32 v183, v186, 0
	v_lshlrev_b32_e32 v190, 16, v183
	v_sub_f32_e32 v190, v186, v190
	v_cvt_pk_bf16_f32 v192, v190, 0
	v_cvt_pk_bf16_f32 v190, v187, 0
	v_lshlrev_b32_e32 v190, 16, v190
	v_sub_f32_e32 v191, v187, v190
	v_cvt_pk_bf16_f32 v193, v191, 0
	v_and_or_b32 v190, v183, s35, v190
	v_lshlrev_b32_e32 v183, 16, v193
	v_mov_b32_e32 v193, v1
	v_pk_fma_f32 v[188:189], v[12:13], v[188:189], v[20:21]
	v_cvt_pk_fp8_f32 v193, v186, v187
	v_pk_fma_f32 v[188:189], v[140:141], v[188:189], v[144:145]
	s_add_u32 s12, s20, s12
	v_cvt_pk_bf16_f32 v216, v189, 0
	v_cvt_pk_bf16_f32 v191, v188, 0
	v_lshlrev_b32_e32 v216, 16, v216
	v_lshlrev_b32_e32 v209, 16, v191
	v_sub_f32_e32 v217, v189, v216
	v_cvt_pk_fp8_f32 v193, v188, v189 op_sel:[0,0,1]
	v_sub_f32_e32 v209, v188, v209
	v_cvt_pk_bf16_f32 v217, v217, 0
	v_cvt_pk_bf16_f32 v209, v209, 0
	v_and_or_b32 v186, v192, s35, v183
	v_lshlrev_b32_e32 v183, 16, v217
	s_addc_u32 s13, s21, s13
	v_and_or_b32 v191, v191, s35, v216
	v_and_or_b32 v187, v209, s35, v183
	v_lshl_add_u64 v[188:189], s[12:13], 0, v[0:1]
	v_add_u32_e32 v183, s47, v235
	global_store_dword v[188:189], v193, off
	ds_write_b64 v183, v[190:191]
	ds_write_b64 v183, v[186:187] offset:33024
	v_pk_mul_f32 v[186:187], v[246:247], v[182:183] op_sel_hi:[1,0]
	v_pk_mul_f32 v[184:185], v[184:185], v[182:183] op_sel_hi:[1,0]
	s_waitcnt vmcnt(20)
	v_pk_fma_f32 v[186:187], v[14:15], v[186:187], v[22:23]
	v_pk_fma_f32 v[184:185], v[16:17], v[184:185], v[24:25]
	v_pk_fma_f32 v[186:187], v[150:151], v[186:187], v[146:147]
	v_pk_fma_f32 v[184:185], v[152:153], v[184:185], v[148:149]
	v_cvt_pk_bf16_f32 v183, v186, 0
	v_lshlrev_b32_e32 v188, 16, v183
	v_sub_f32_e32 v188, v186, v188
	v_cvt_pk_bf16_f32 v209, v188, 0
	v_cvt_pk_bf16_f32 v188, v187, 0
	v_lshlrev_b32_e32 v218, 16, v188
	v_sub_f32_e32 v188, v187, v218
	v_cvt_pk_bf16_f32 v246, v184, 0
	v_cvt_pk_bf16_f32 v219, v188, 0
	v_lshlrev_b32_e32 v188, 16, v246
	v_sub_f32_e32 v188, v184, v188
	v_cvt_pk_bf16_f32 v247, v188, 0
	v_mov_b32_e32 v188, v175
	v_mov_b32_e32 v189, v176
	v_mov_b32_e32 v190, v174
	v_mov_b32_e32 v191, v177
	v_pk_add_f32 v[188:189], v[188:189], v[190:191]
	v_mov_b32_e32 v190, v171
	v_mov_b32_e32 v191, v172
	v_mov_b32_e32 v192, v170
	v_mov_b32_e32 v193, v173
	v_pk_add_f32 v[190:191], v[190:191], v[192:193]
	v_add_f32_e32 v188, v188, v189
	v_pk_add_f32 v[190:191], v[190:191], v[190:191] op_sel:[0,1] op_sel_hi:[1,0]
	v_add_f32_e32 v188, 0, v188
	v_add_f32_e32 v192, v166, v167
	v_add_f32_e32 v216, v168, v169
	v_mov_b32_e32 v189, v162
	v_mov_b32_e32 v191, v163
	v_mov_b32_e32 v193, v164
	v_mov_b32_e32 v217, v165
	v_pk_add_f32 v[188:189], v[188:189], v[190:191]
	v_pk_add_f32 v[190:191], v[192:193], v[216:217]
	v_cvt_pk_bf16_f32 v248, v185, 0
	v_pk_add_f32 v[188:189], v[188:189], v[190:191]
	v_lshlrev_b32_e32 v191, 16, v248
	v_add_f32_e32 v189, v188, v189
	s_nop 1
	v_add_f32_dpp v189, v189, v189 quad_perm:[1,0,3,2] row_mask:0xf bank_mask:0xf
	s_nop 1
	v_add_f32_dpp v189, v189, v189 quad_perm:[2,3,0,1] row_mask:0xf bank_mask:0xf
	s_nop 1
	v_add_f32_dpp v189, v189, v189 row_half_mirror row_mask:0xf bank_mask:0xf
	s_nop 1
	v_add_f32_dpp v189, v189, v189 row_mirror row_mask:0xf bank_mask:0xf
	v_mov_b32_e32 v190, v189
	s_nop 1
	v_permlane16_swap_b32_e32 v190, v189
	s_nop 1
	v_add_f32_e32 v189, v189, v190
	v_mov_b32_e32 v190, v189
	s_nop 1
	v_permlane32_swap_b32_e32 v190, v189
	s_nop 1
	v_add_f32_e32 v189, v189, v190
	v_sub_f32_e32 v188, v185, v191
	v_cvt_pk_bf16_f32 v192, v188, 0
	v_and_or_b32 v188, v183, s35, v218
	v_mov_b32_e32 v193, v1
	s_waitcnt lgkmcnt(0)
	v_mov_b32_e32 v183, v189
	v_cvt_pk_fp8_f32 v193, v186, v187
	v_and_or_b32 v189, v246, s35, v191
	v_lshlrev_b32_e32 v191, 16, v219
	v_and_or_b32 v186, v209, s35, v191
	s_waitcnt lgkmcnt(0)
	v_cvt_pk_fp8_f32 v193, v184, v185 op_sel:[0,0,1]
	v_lshl_add_u64 v[184:185], s[12:13], 0, v[198:199]
	v_lshlrev_b32_e32 v187, 16, v192
	v_and_or_b32 v187, v247, s35, v187
	s_waitcnt lgkmcnt(0)
	global_store_dword v[184:185], v193, off
	v_add_u32_e32 v184, s47, v236
	ds_write_b64 v184, v[188:189]
	ds_write_b64 v184, v[186:187] offset:33024
	s_waitcnt lgkmcnt(2)
	v_pk_mul_f32 v[180:181], v[180:181], v[182:183] op_sel_hi:[1,0]
	v_pk_mul_f32 v[178:179], v[178:179], v[182:183] op_sel_hi:[1,0]
	s_waitcnt vmcnt(19)
	v_pk_fma_f32 v[180:181], v[28:29], v[180:181], v[32:33]
	v_pk_fma_f32 v[178:179], v[26:27], v[178:179], v[30:31]
	s_waitcnt lgkmcnt(0)
	v_mov_b32_e32 v182, v183
	s_waitcnt vmcnt(3)
	v_pk_fma_f32 v[180:181], v[156:157], v[180:181], v[160:161]
	v_pk_fma_f32 v[178:179], v[154:155], v[178:179], v[158:159]
	s_waitcnt lgkmcnt(0)
	v_mov_b32_e32 v191, v182
	v_fmamk_f32 v175, v191, 0xba800000, v175
	v_fmamk_f32 v174, v191, 0xba800000, v174
	v_fmamk_f32 v177, v191, 0xba800000, v177
	v_fmac_f32_e32 v176, 0xba800000, v191
	v_pk_mul_f32 v[182:183], v[176:177], v[176:177]
	v_pk_mul_f32 v[184:185], v[174:175], v[174:175]
	v_fmamk_f32 v171, v191, 0xba800000, v171
	v_pk_mov_b32 v[186:187], v[184:185], v[182:183] op_sel:[1,0]
	v_mov_b32_e32 v185, v183
	v_pk_add_f32 v[182:183], v[186:187], v[184:185]
	v_fmamk_f32 v170, v191, 0xba800000, v170
	v_fmamk_f32 v173, v191, 0xba800000, v173
	v_fmac_f32_e32 v172, 0xba800000, v191
	v_pk_add_f32 v[182:183], v[182:183], v[182:183] op_sel_hi:[0,1]
	v_pk_mul_f32 v[184:185], v[172:173], v[172:173]
	v_pk_mul_f32 v[186:187], v[170:171], v[170:171]
	v_fmamk_f32 v166, v191, 0xba800000, v166
	v_pk_mov_b32 v[188:189], v[186:187], v[184:185] op_sel:[1,0]
	v_mov_b32_e32 v187, v185
	v_fmamk_f32 v167, v191, 0xba800000, v167
	v_fmac_f32_e32 v168, 0xba800000, v191
	v_mul_f32_e32 v182, v166, v166
	v_pk_add_f32 v[184:185], v[188:189], v[186:187]
	v_fmamk_f32 v169, v191, 0xba800000, v169
	v_pk_fma_f32 v[186:187], v[166:167], v[166:167], v[182:183] op_sel_hi:[1,1,0]
	v_mul_f32_e32 v182, v168, v168
	v_pk_add_f32 v[184:185], v[184:185], v[184:185] op_sel_hi:[0,1]
	v_pk_fma_f32 v[188:189], v[168:169], v[168:169], v[182:183] op_sel_hi:[1,1,0]
	v_fmamk_f32 v165, v191, 0xba800000, v165
	v_fmamk_f32 v164, v191, 0xba800000, v164
	v_fmamk_f32 v163, v191, 0xba800000, v163
	v_fmac_f32_e32 v162, 0xba800000, v191
	v_mul_f32_e32 v186, v162, v162
	v_mul_f32_e32 v188, v163, v163
	v_mul_f32_e32 v182, v164, v164
	v_mul_f32_e32 v184, v165, v165
	v_pk_add_f32 v[186:187], v[186:187], v[188:189]
	v_pk_add_f32 v[182:183], v[182:183], v[184:185]
	v_cvt_pk_bf16_f32 v189, v181, 0
	v_pk_add_f32 v[182:183], v[186:187], v[182:183]
	v_cvt_pk_bf16_f32 v185, v179, 0
	v_add_f32_e32 v182, v182, v183
	s_nop 1
	v_add_f32_dpp v182, v182, v182 quad_perm:[1,0,3,2] row_mask:0xf bank_mask:0xf
	s_nop 1
	v_add_f32_dpp v182, v182, v182 quad_perm:[2,3,0,1] row_mask:0xf bank_mask:0xf
	s_nop 1
	v_add_f32_dpp v182, v182, v182 row_half_mirror row_mask:0xf bank_mask:0xf
	s_nop 1
	v_add_f32_dpp v182, v182, v182 row_mirror row_mask:0xf bank_mask:0xf
	v_mov_b32_e32 v183, v182
	s_nop 1
	v_permlane16_swap_b32_e32 v183, v182
	s_nop 1
	v_add_f32_e32 v182, v182, v183
	v_mov_b32_e32 v183, v182
	s_nop 1
	v_permlane32_swap_b32_e32 v183, v182
	s_nop 1
	v_add_f32_e32 v182, v182, v183
	v_lshlrev_b32_e32 v189, 16, v189
	v_cvt_pk_bf16_f32 v190, v178, 0
	v_lshlrev_b32_e32 v185, 16, v185
	v_sub_f32_e32 v186, v179, v185
	s_waitcnt lgkmcnt(0)
	v_lshlrev_b32_e32 v184, 16, v190
	v_cvt_pk_bf16_f32 v187, v180, 0
	v_lshlrev_b32_e32 v188, 16, v187
	v_sub_f32_e32 v188, v180, v188
	s_waitcnt lgkmcnt(0)
	v_sub_f32_e32 v184, v178, v184
	v_cvt_pk_bf16_f32 v186, v186, 0
	v_cvt_pk_bf16_f32 v184, v184, 0
	v_lshlrev_b32_e32 v186, 16, v186
	s_waitcnt lgkmcnt(0)
	v_mov_b32_e32 v183, v182
	v_sub_f32_e32 v182, v181, v189
	v_cvt_pk_bf16_f32 v192, v182, 0
	v_and_or_b32 v182, v190, s35, v185
	v_cvt_pk_bf16_f32 v188, v188, 0
	s_waitcnt lgkmcnt(0)
	v_mov_b32_e32 v185, v183
	v_and_or_b32 v183, v187, s35, v189
	v_mov_b32_e32 v187, v1
	v_cvt_pk_fp8_f32 v187, v178, v179
	v_and_or_b32 v178, v184, s35, v186
	s_waitcnt lgkmcnt(0)
	v_cvt_pk_fp8_f32 v187, v180, v181 op_sel:[0,0,1]
	v_lshlrev_b32_e32 v179, 16, v192
	v_and_or_b32 v179, v188, s35, v179
	s_waitcnt lgkmcnt(0)
	v_mov_b32_e32 v180, v185
	v_fmamk_f32 v180, v180, 0x3a800000, v211
	v_mul_f32_e32 v181, 0x4f800000, v180
	v_cmp_gt_f32_e32 vcc, s36, v180
	s_nop 1
	v_cndmask_b32_e32 v184, v180, v181, vcc
	v_sqrt_f32_e32 v185, v184
	v_lshl_add_u64 v[180:181], s[12:13], 0, v[200:201]
	global_store_dword v[180:181], v187, off
	v_add_u32_e32 v180, s47, v237
	v_add_u32_e32 v181, -1, v185
	v_fma_f32 v186, -v181, v185, v184
	v_cmp_ge_f32_e64 s[12:13], 0, v186
	v_add_u32_e32 v186, 1, v185
	ds_write_b64 v180, v[182:183]
	ds_write_b64 v180, v[178:179] offset:33024
	v_cndmask_b32_e64 v181, v185, v181, s[12:13]
	v_fma_f32 v185, -v186, v185, v184
	v_cmp_lt_f32_e64 s[12:13], 0, v185
	s_nop 1
	v_cndmask_b32_e64 v181, v181, v186, s[12:13]
	v_mul_f32_e32 v185, 0x37800000, v181
	v_cndmask_b32_e32 v181, v181, v185, vcc
	v_cmp_class_f32_e32 vcc, v184, v212
	s_nop 1
	v_cndmask_b32_e32 v181, v181, v184, vcc
	v_div_scale_f32 v184, s[12:13], v181, v181, 1.0
	v_rcp_f32_e32 v185, v184
	s_add_i32 s12, s34, 1
	s_ashr_i32 s13, s12, 31
	s_lshl_b64 s[12:13], s[12:13], 10
	v_fma_f32 v178, -v184, v185, 1.0
	v_fmac_f32_e32 v185, v178, v185
	v_div_scale_f32 v178, vcc, 1.0, v181, 1.0
	v_mul_f32_e32 v179, v178, v185
	v_fma_f32 v180, -v184, v179, v178
	v_fmac_f32_e32 v179, v180, v185
	v_fma_f32 v178, -v184, v179, v178
	v_div_fmas_f32 v178, v178, v185, v179
	v_div_fixup_f32 v178, v178, v181, 1.0
	v_pk_mul_f32 v[174:175], v[174:175], v[178:179] op_sel_hi:[1,0]
	v_pk_mul_f32 v[176:177], v[176:177], v[178:179] op_sel_hi:[1,0]
	v_pk_fma_f32 v[174:175], v[2:3], v[174:175], v[6:7]
	v_pk_fma_f32 v[176:177], v[4:5], v[176:177], v[8:9]
	v_pk_fma_f32 v[174:175], v[98:99], v[174:175], v[118:119]
	v_pk_fma_f32 v[176:177], v[100:101], v[176:177], v[120:121]
	v_cvt_pk_bf16_f32 v179, v174, 0
	v_lshlrev_b32_e32 v180, 16, v179
	v_sub_f32_e32 v180, v174, v180
	v_cvt_pk_bf16_f32 v182, v180, 0
	v_cvt_pk_bf16_f32 v180, v175, 0
	v_lshlrev_b32_e32 v180, 16, v180
	v_sub_f32_e32 v181, v175, v180
	v_and_or_b32 v180, v179, s35, v180
	v_mov_b32_e32 v179, v1
	v_cvt_pk_fp8_f32 v179, v174, v175
	v_cvt_pk_bf16_f32 v185, v177, 0
	v_cvt_pk_bf16_f32 v183, v181, 0
	v_cvt_pk_bf16_f32 v181, v176, 0
	v_cvt_pk_fp8_f32 v179, v176, v177 op_sel:[0,0,1]
	v_lshlrev_b32_e32 v185, 16, v185
	v_lshlrev_b32_e32 v184, 16, v181
	v_sub_f32_e32 v186, v177, v185
	v_pk_mul_f32 v[170:171], v[170:171], v[178:179] op_sel_hi:[1,0]
	v_sub_f32_e32 v184, v176, v184
	v_cvt_pk_bf16_f32 v186, v186, 0
	v_lshlrev_b32_e32 v174, 16, v183
	v_lshl_add_u64 v[176:177], v[202:203], 0, s[12:13]
	v_pk_fma_f32 v[170:171], v[10:11], v[170:171], v[18:19]
	v_cvt_pk_bf16_f32 v184, v184, 0
	v_and_or_b32 v181, v181, s35, v185
	v_and_or_b32 v174, v182, s35, v174
	v_lshlrev_b32_e32 v175, 16, v186
	global_store_dword v[176:177], v179, off
	v_add_u32_e32 v176, s48, v234
	v_pk_fma_f32 v[170:171], v[138:139], v[170:171], v[142:143]
	v_and_or_b32 v175, v184, s35, v175
	ds_write_b64 v176, v[180:181]
	ds_write_b64 v176, v[174:175] offset:33024
	v_pk_mul_f32 v[172:173], v[172:173], v[178:179] op_sel_hi:[1,0]
	v_cvt_pk_bf16_f32 v174, v170, 0
	v_pk_fma_f32 v[172:173], v[12:13], v[172:173], v[20:21]
	v_lshlrev_b32_e32 v175, 16, v174
	v_pk_fma_f32 v[172:173], v[140:141], v[172:173], v[144:145]
	v_sub_f32_e32 v175, v170, v175
	v_cvt_pk_bf16_f32 v176, v175, 0
	v_cvt_pk_bf16_f32 v175, v171, 0
	v_cvt_pk_bf16_f32 v181, v173, 0
	v_lshlrev_b32_e32 v175, 16, v175
	v_cvt_pk_bf16_f32 v179, v172, 0
	v_lshlrev_b32_e32 v181, 16, v181
	v_sub_f32_e32 v177, v171, v175
	v_lshlrev_b32_e32 v180, 16, v179
	v_and_or_b32 v174, v174, s35, v175
	v_and_or_b32 v175, v179, s35, v181
	v_mov_b32_e32 v179, v1
	v_cvt_pk_fp8_f32 v179, v170, v171
	s_add_u32 s12, s20, s12
	s_addc_u32 s13, s21, s13
	v_sub_f32_e32 v180, v172, v180
	v_cvt_pk_fp8_f32 v179, v172, v173 op_sel:[0,0,1]
	v_sub_f32_e32 v182, v173, v181
	v_lshl_add_u64 v[172:173], s[12:13], 0, v[0:1]
	v_cvt_pk_bf16_f32 v177, v177, 0
	v_pk_mul_f32 v[166:167], v[166:167], v[178:179] op_sel_hi:[1,0]
	global_store_dword v[172:173], v179, off
	v_pk_fma_f32 v[166:167], v[14:15], v[166:167], v[22:23]
	v_pk_mul_f32 v[168:169], v[168:169], v[178:179] op_sel_hi:[1,0]
	v_pk_fma_f32 v[166:167], v[150:151], v[166:167], v[146:147]
	v_mov_b32_e32 v179, v1
	v_cvt_pk_bf16_f32 v182, v182, 0
	v_lshlrev_b32_e32 v177, 16, v177
	v_cvt_pk_fp8_f32 v179, v166, v167
	v_cvt_pk_bf16_f32 v180, v180, 0
	v_and_or_b32 v170, v176, s35, v177
	v_lshlrev_b32_e32 v171, 16, v182
	v_add_u32_e32 v172, s48, v235
	v_and_or_b32 v171, v180, s35, v171
	ds_write_b64 v172, v[174:175]
	ds_write_b64 v172, v[170:171] offset:33024
	v_pk_fma_f32 v[168:169], v[16:17], v[168:169], v[24:25]
	v_cvt_pk_bf16_f32 v170, v166, 0
	v_pk_fma_f32 v[168:169], v[152:153], v[168:169], v[148:149]
	v_lshlrev_b32_e32 v171, 16, v170
	v_sub_f32_e32 v171, v166, v171
	v_cvt_pk_fp8_f32 v179, v168, v169 op_sel:[0,0,1]
	v_cvt_pk_bf16_f32 v172, v171, 0
	v_cvt_pk_bf16_f32 v171, v167, 0
	v_lshlrev_b32_e32 v171, 16, v171
	v_cvt_pk_bf16_f32 v176, v169, 0
	v_sub_f32_e32 v173, v167, v171
	v_cvt_pk_bf16_f32 v174, v168, 0
	v_lshlrev_b32_e32 v176, 16, v176
	v_cvt_pk_bf16_f32 v173, v173, 0
	v_lshlrev_b32_e32 v175, 16, v174
	v_sub_f32_e32 v177, v169, v176
	v_pk_mul_f32 v[162:163], v[162:163], v[178:179] op_sel_hi:[1,0]
	v_sub_f32_e32 v175, v168, v175
	v_cvt_pk_bf16_f32 v177, v177, 0
	v_lshlrev_b32_e32 v166, 16, v173
	v_lshl_add_u64 v[168:169], s[12:13], 0, v[198:199]
	v_pk_fma_f32 v[162:163], v[26:27], v[162:163], v[30:31]
	v_cvt_pk_bf16_f32 v175, v175, 0
	v_and_or_b32 v170, v170, s35, v171
	v_and_or_b32 v171, v174, s35, v176
	v_and_or_b32 v166, v172, s35, v166
	v_lshlrev_b32_e32 v167, 16, v177
	global_store_dword v[168:169], v179, off
	v_add_u32_e32 v168, s48, v236
	v_pk_fma_f32 v[162:163], v[154:155], v[162:163], v[158:159]
	v_mov_b32_e32 v174, v1
	v_and_or_b32 v167, v175, s35, v167
	ds_write_b64 v168, v[170:171]
	ds_write_b64 v168, v[166:167] offset:33024
	v_pk_mul_f32 v[164:165], v[164:165], v[178:179] op_sel_hi:[1,0]
	v_cvt_pk_bf16_f32 v166, v162, 0
	v_cvt_pk_fp8_f32 v174, v162, v163
	v_pk_fma_f32 v[164:165], v[28:29], v[164:165], v[32:33]
	v_lshlrev_b32_e32 v167, 16, v166
	v_pk_fma_f32 v[164:165], v[156:157], v[164:165], v[160:161]
	v_sub_f32_e32 v167, v162, v167
	v_cvt_pk_bf16_f32 v168, v167, 0
	v_cvt_pk_bf16_f32 v167, v163, 0
	v_cvt_pk_bf16_f32 v172, v165, 0
	v_lshlrev_b32_e32 v167, 16, v167
	v_cvt_pk_bf16_f32 v170, v164, 0
	v_lshlrev_b32_e32 v172, 16, v172
	v_cvt_pk_fp8_f32 v174, v164, v165 op_sel:[0,0,1]
	v_sub_f32_e32 v169, v163, v167
	v_lshlrev_b32_e32 v171, 16, v170
	v_sub_f32_e32 v173, v165, v172
	v_cvt_pk_bf16_f32 v169, v169, 0
	v_sub_f32_e32 v171, v164, v171
	v_cvt_pk_bf16_f32 v173, v173, 0
	v_cvt_pk_bf16_f32 v171, v171, 0
	v_lshlrev_b32_e32 v162, 16, v169
	v_lshlrev_b32_e32 v163, 16, v173
	v_lshl_add_u64 v[164:165], s[12:13], 0, v[200:201]
	v_and_or_b32 v166, v166, s35, v167
	v_and_or_b32 v167, v170, s35, v172
	v_and_or_b32 v162, v168, s35, v162
	v_and_or_b32 v163, v171, s35, v163
	global_store_dword v[164:165], v174, off
	v_add_u32_e32 v164, s48, v237
	ds_write_b64 v164, v[166:167]
	ds_write_b64 v164, v[162:163] offset:33024
	s_waitcnt lgkmcnt(0)
	s_barrier
	ds_read_b128 v[162:165], v238
	ds_read_b128 v[166:169], v238 offset:64
	s_waitcnt lgkmcnt(1)
	v_mfma_f32_16x16x32_bf16 v[170:173], v[162:165], v[34:37], 0
	ds_read_b128 v[174:177], v238 offset:33024
	ds_read_b128 v[178:181], v238 offset:33088
	s_mov_b64 s[34:35], -1
	s_mov_b64 s[12:13], -1
	v_mfma_f32_16x16x32_bf16 v[182:185], v[162:165], v[42:45], 0
	s_waitcnt lgkmcnt(1)
	v_mfma_f32_16x16x32_bf16 v[170:173], v[174:177], v[34:37], v[170:173]
	v_mfma_f32_16x16x32_bf16 v[174:177], v[174:177], v[42:45], v[182:185]
	v_mfma_f32_16x16x32_bf16 v[170:173], v[162:165], v[38:41], v[170:173]
	v_mfma_f32_16x16x32_bf16 v[162:165], v[162:165], v[46:49], v[174:177]
	v_mfma_f32_16x16x32_bf16 v[170:173], v[166:169], v[50:53], v[170:173]
	v_mfma_f32_16x16x32_bf16 v[162:165], v[166:169], v[58:61], v[162:165]
	s_waitcnt lgkmcnt(0)
	v_mfma_f32_16x16x32_bf16 v[170:173], v[178:181], v[50:53], v[170:173]
	v_mfma_f32_16x16x32_bf16 v[162:165], v[178:181], v[58:61], v[162:165]
	v_mfma_f32_16x16x32_bf16 v[170:173], v[166:169], v[54:57], v[170:173]
	v_mfma_f32_16x16x32_bf16 v[162:165], v[166:169], v[62:65], v[162:165]
	ds_read_b128 v[166:169], v238 offset:128
	ds_read_b128 v[174:177], v238 offset:192
	ds_read_b128 v[178:181], v238 offset:33152
	ds_read_b128 v[182:185], v238 offset:33216
	s_waitcnt lgkmcnt(3)
	v_mfma_f32_16x16x32_bf16 v[170:173], v[166:169], v[66:69], v[170:173]
	v_mfma_f32_16x16x32_bf16 v[162:165], v[166:169], v[74:77], v[162:165]
	s_waitcnt lgkmcnt(1)
	v_mfma_f32_16x16x32_bf16 v[170:173], v[178:181], v[66:69], v[170:173]
	v_mfma_f32_16x16x32_bf16 v[162:165], v[178:181], v[74:77], v[162:165]
	v_mfma_f32_16x16x32_bf16 v[170:173], v[166:169], v[70:73], v[170:173]
	v_mfma_f32_16x16x32_bf16 v[162:165], v[166:169], v[78:81], v[162:165]
	v_mfma_f32_16x16x32_bf16 v[166:169], v[174:177], v[82:85], v[170:173]
	v_mfma_f32_16x16x32_bf16 v[162:165], v[174:177], v[90:93], v[162:165]
	s_waitcnt lgkmcnt(0)
	v_mfma_f32_16x16x32_bf16 v[166:169], v[182:185], v[82:85], v[166:169]
	v_mfma_f32_16x16x32_bf16 v[162:165], v[182:185], v[90:93], v[162:165]
	v_mfma_f32_16x16x32_bf16 v[166:169], v[174:177], v[86:89], v[166:169]
	v_mfma_f32_16x16x32_bf16 v[162:165], v[174:177], v[94:97], v[162:165]
	s_nop 7
	ds_write2_b32 v239, v166, v162 offset1:16
	ds_write2_b32 v239, v167, v163 offset0:32 offset1:48
	ds_write2_b32 v239, v168, v164 offset0:64 offset1:80
	ds_write2_b32 v239, v169, v165 offset0:96 offset1:112
	s_waitcnt lgkmcnt(0)
	s_barrier
	ds_read2st64_b32 v[162:163], v233 offset1:8
	ds_read2st64_b32 v[164:165], v233 offset0:16 offset1:24
	s_waitcnt lgkmcnt(1)
	v_add_f32_e32 v162, v242, v162
	ds_read2st64_b32 v[166:167], v233 offset0:32 offset1:40
	v_add_f32_e32 v168, v162, v163
	ds_read2st64_b32 v[162:163], v233 offset0:48 offset1:56
	s_waitcnt lgkmcnt(2)
	v_add_f32_e32 v164, v168, v164
	v_add_f32_e32 v164, v164, v165
	s_waitcnt lgkmcnt(1)
	v_add_f32_e32 v164, v164, v166
	v_add_f32_e32 v164, v164, v167
	s_waitcnt lgkmcnt(0)
	v_add_f32_e32 v162, v164, v162
	v_add_f32_e32 v165, v162, v163
	ds_bpermute_b32 v162, v230, v165
	ds_bpermute_b32 v163, v230, v232
	s_waitcnt lgkmcnt(1)
	v_cmp_nlt_f32_e32 vcc, v165, v162
	s_and_saveexec_b64 s[36:37], vcc
	s_cbranch_execz .LBB0_988
	v_cmp_eq_f32_e32 vcc, v165, v162
	s_waitcnt lgkmcnt(0)
	v_cmp_lt_i32_e64 s[12:13], v163, v232
	s_and_b64 s[12:13], vcc, s[12:13]
	s_orn2_b64 s[12:13], s[12:13], exec
